# speedup vs baseline: 1.0069x; 1.0065x over previous
_Z6k_bcsrPK15HIP_vector_typeIiLj2EEPKiPiS5_:
	s_load_dwordx8 s[4:11], s[0:1], 0x0
	v_lshlrev_b32_e32 v1, 2, v0
	v_mov_b32_e32 v2, 0
	ds_write_b32 v1, v2
	ds_write_b32 v1, v2 offset:1024
	s_lshl_b32 s3, s2, 2
	s_waitcnt lgkmcnt(0)
	s_add_u32 s12, s6, s3
	s_addc_u32 s13, s7, 0
	s_load_dwordx2 s[14:15], s[12:13], 0x0
	s_lshl_b32 s16, s2, 9
	s_sub_u32 s17, s2, 0x30e
	s_lshl_b32 s17, s17, 6
	s_add_u32 s17, s17, 0x61a80
	s_cmpk_lt_u32 s2, 0x30e
	s_cselect_b32 s20, s16, s17
	s_mov_b32 s18, 0x668a0
	s_cselect_b32 s18, 0x61a80, s18
	s_cselect_b32 s19, 0x200, 64
	s_sub_u32 s22, s18, s20
	s_min_u32 s22, s22, s19
	s_waitcnt lgkmcnt(0)
	s_sub_u32 s21, s15, s14
	s_barrier
	s_mov_b32 s30, 0
	s_cmp_gt_u32 s21, 0x1000
	s_cbranch_scc1 .Lbc_slow1
	v_add_u32_e32 v3, s14, v0
	v_lshlrev_b32_e32 v3, 3, v3
	v_mov_b32_e32 v17, -1
	v_mov_b32_e32 v48, -1
	v_mov_b32_e32 v19, -1
	v_mov_b32_e32 v49, -1
	v_mov_b32_e32 v21, -1
	v_mov_b32_e32 v50, -1
	v_mov_b32_e32 v23, -1
	v_mov_b32_e32 v51, -1
	v_mov_b32_e32 v25, -1
	v_mov_b32_e32 v52, -1
	v_mov_b32_e32 v27, -1
	v_mov_b32_e32 v53, -1
	v_mov_b32_e32 v29, -1
	v_mov_b32_e32 v54, -1
	v_mov_b32_e32 v31, -1
	v_mov_b32_e32 v55, -1
	v_mov_b32_e32 v33, -1
	v_mov_b32_e32 v56, -1
	v_mov_b32_e32 v35, -1
	v_mov_b32_e32 v57, -1
	v_mov_b32_e32 v37, -1
	v_mov_b32_e32 v58, -1
	v_mov_b32_e32 v39, -1
	v_mov_b32_e32 v59, -1
	v_mov_b32_e32 v41, -1
	v_mov_b32_e32 v60, -1
	v_mov_b32_e32 v43, -1
	v_mov_b32_e32 v61, -1
	v_mov_b32_e32 v45, -1
	v_mov_b32_e32 v62, -1
	v_mov_b32_e32 v47, -1
	v_mov_b32_e32 v63, -1
	s_cmp_lt_u32 0, s21
	s_cbranch_scc0 .Lbc_ld_done
	v_add_u32_e32 v4, 0x0, v0
	v_cmp_gt_u32_e32 vcc, s21, v4
	s_and_saveexec_b64 s[32:33], vcc
	global_load_dwordx2 v[16:17], v3, s[4:5] nt
	s_mov_b64 exec, s[32:33]
	s_cmp_lt_u32 0x100, s21
	s_cbranch_scc0 .Lbc_ld_done
	v_add_u32_e32 v4, 0x100, v0
	v_cmp_gt_u32_e32 vcc, s21, v4
	s_and_saveexec_b64 s[32:33], vcc
	v_add_u32_e32 v5, 0x800, v3
	global_load_dwordx2 v[18:19], v5, s[4:5] nt
	s_mov_b64 exec, s[32:33]
	s_cmp_lt_u32 0x200, s21
	s_cbranch_scc0 .Lbc_ld_done
	v_add_u32_e32 v4, 0x200, v0
	v_cmp_gt_u32_e32 vcc, s21, v4
	s_and_saveexec_b64 s[32:33], vcc
	v_add_u32_e32 v5, 0x1000, v3
	global_load_dwordx2 v[20:21], v5, s[4:5] nt
	s_mov_b64 exec, s[32:33]
	s_cmp_lt_u32 0x300, s21
	s_cbranch_scc0 .Lbc_ld_done
	v_add_u32_e32 v4, 0x300, v0
	v_cmp_gt_u32_e32 vcc, s21, v4
	s_and_saveexec_b64 s[32:33], vcc
	v_add_u32_e32 v5, 0x1800, v3
	global_load_dwordx2 v[22:23], v5, s[4:5] nt
	s_mov_b64 exec, s[32:33]
	s_cmp_lt_u32 0x400, s21
	s_cbranch_scc0 .Lbc_ld_done
	v_add_u32_e32 v4, 0x400, v0
	v_cmp_gt_u32_e32 vcc, s21, v4
	s_and_saveexec_b64 s[32:33], vcc
	v_add_u32_e32 v5, 0x2000, v3
	global_load_dwordx2 v[24:25], v5, s[4:5] nt
	s_mov_b64 exec, s[32:33]
	s_cmp_lt_u32 0x500, s21
	s_cbranch_scc0 .Lbc_ld_done
	v_add_u32_e32 v4, 0x500, v0
	v_cmp_gt_u32_e32 vcc, s21, v4
	s_and_saveexec_b64 s[32:33], vcc
	v_add_u32_e32 v5, 0x2800, v3
	global_load_dwordx2 v[26:27], v5, s[4:5] nt
	s_mov_b64 exec, s[32:33]
	s_cmp_lt_u32 0x600, s21
	s_cbranch_scc0 .Lbc_ld_done
	v_add_u32_e32 v4, 0x600, v0
	v_cmp_gt_u32_e32 vcc, s21, v4
	s_and_saveexec_b64 s[32:33], vcc
	v_add_u32_e32 v5, 0x3000, v3
	global_load_dwordx2 v[28:29], v5, s[4:5] nt
	s_mov_b64 exec, s[32:33]
	s_cmp_lt_u32 0x700, s21
	s_cbranch_scc0 .Lbc_ld_done
	v_add_u32_e32 v4, 0x700, v0
	v_cmp_gt_u32_e32 vcc, s21, v4
	s_and_saveexec_b64 s[32:33], vcc
	v_add_u32_e32 v5, 0x3800, v3
	global_load_dwordx2 v[30:31], v5, s[4:5] nt
	s_mov_b64 exec, s[32:33]
	s_cmp_lt_u32 0x800, s21
	s_cbranch_scc0 .Lbc_ld_done
	v_add_u32_e32 v4, 0x800, v0
	v_cmp_gt_u32_e32 vcc, s21, v4
	s_and_saveexec_b64 s[32:33], vcc
	v_add_u32_e32 v5, 0x4000, v3
	global_load_dwordx2 v[32:33], v5, s[4:5] nt
	s_mov_b64 exec, s[32:33]
	s_cmp_lt_u32 0x900, s21
	s_cbranch_scc0 .Lbc_ld_done
	v_add_u32_e32 v4, 0x900, v0
	v_cmp_gt_u32_e32 vcc, s21, v4
	s_and_saveexec_b64 s[32:33], vcc
	v_add_u32_e32 v5, 0x4800, v3
	global_load_dwordx2 v[34:35], v5, s[4:5] nt
	s_mov_b64 exec, s[32:33]
	s_cmp_lt_u32 0xa00, s21
	s_cbranch_scc0 .Lbc_ld_done
	v_add_u32_e32 v4, 0xa00, v0
	v_cmp_gt_u32_e32 vcc, s21, v4
	s_and_saveexec_b64 s[32:33], vcc
	v_add_u32_e32 v5, 0x5000, v3
	global_load_dwordx2 v[36:37], v5, s[4:5] nt
	s_mov_b64 exec, s[32:33]
	s_cmp_lt_u32 0xb00, s21
	s_cbranch_scc0 .Lbc_ld_done
	v_add_u32_e32 v4, 0xb00, v0
	v_cmp_gt_u32_e32 vcc, s21, v4
	s_and_saveexec_b64 s[32:33], vcc
	v_add_u32_e32 v5, 0x5800, v3
	global_load_dwordx2 v[38:39], v5, s[4:5] nt
	s_mov_b64 exec, s[32:33]
	s_cmp_lt_u32 0xc00, s21
	s_cbranch_scc0 .Lbc_ld_done
	v_add_u32_e32 v4, 0xc00, v0
	v_cmp_gt_u32_e32 vcc, s21, v4
	s_and_saveexec_b64 s[32:33], vcc
	v_add_u32_e32 v5, 0x6000, v3
	global_load_dwordx2 v[40:41], v5, s[4:5] nt
	s_mov_b64 exec, s[32:33]
	s_cmp_lt_u32 0xd00, s21
	s_cbranch_scc0 .Lbc_ld_done
	v_add_u32_e32 v4, 0xd00, v0
	v_cmp_gt_u32_e32 vcc, s21, v4
	s_and_saveexec_b64 s[32:33], vcc
	v_add_u32_e32 v5, 0x6800, v3
	global_load_dwordx2 v[42:43], v5, s[4:5] nt
	s_mov_b64 exec, s[32:33]
	s_cmp_lt_u32 0xe00, s21
	s_cbranch_scc0 .Lbc_ld_done
	v_add_u32_e32 v4, 0xe00, v0
	v_cmp_gt_u32_e32 vcc, s21, v4
	s_and_saveexec_b64 s[32:33], vcc
	v_add_u32_e32 v5, 0x7000, v3
	global_load_dwordx2 v[44:45], v5, s[4:5] nt
	s_mov_b64 exec, s[32:33]
	s_cmp_lt_u32 0xf00, s21
	s_cbranch_scc0 .Lbc_ld_done
	v_add_u32_e32 v4, 0xf00, v0
	v_cmp_gt_u32_e32 vcc, s21, v4
	s_and_saveexec_b64 s[32:33], vcc
	v_add_u32_e32 v5, 0x7800, v3
	global_load_dwordx2 v[46:47], v5, s[4:5] nt
	s_mov_b64 exec, s[32:33]

.Lbc_s1loop:
	v_cmp_gt_u32_e32 vcc, s21, v2
	s_and_b64 exec, exec, vcc
	s_cbranch_execz .Lbc_s1done
	v_add_lshl_u32 v3, v2, s14, 3
	global_load_dwordx2 v[16:17], v3, s[4:5] nt
	v_add_u32_e32 v2, 0x100, v2
	s_waitcnt vmcnt(0)
	v_subrev_u32_e32 v7, s20, v17
	v_lshlrev_b32_e32 v7, 2, v7
	ds_add_u32 v7, v6
	s_branch .Lbc_s1loop

.Lbc_s2loop:
	v_cmp_gt_u32_e32 vcc, s21, v2
	s_and_b64 exec, exec, vcc
	s_cbranch_execz .Lbc_s2done
	v_add_lshl_u32 v3, v2, s14, 3
	global_load_dwordx2 v[16:17], v3, s[4:5] nt
	v_add_u32_e32 v2, 0x100, v2
	s_waitcnt vmcnt(0)
	v_subrev_u32_e32 v7, s20, v17
	v_lshlrev_b32_e32 v7, 2, v7
	ds_add_rtn_u32 v8, v7, v6
	ds_read_b32 v9, v7 offset:2048
	s_waitcnt lgkmcnt(0)
	v_add3_u32 v8, v8, v9, s14
	v_lshlrev_b32_e32 v8, 2, v8
	global_store_dword v8, v16, s[10:11]
	s_branch .Lbc_s2loop

.LBB2_113:
	s_and_b64 vcc, exec, s[4:5]
	s_cbranch_vccz .LBB2_355
	s_lshl_b32 s3, s2, 10
	s_add_i32 s3, s3, 0x136800
	v_or_b32_e32 v2, s3, v0
	s_mov_b32 s3, 0x249eff
	v_cmp_lt_u32_e32 vcc, s3, v2
	s_and_saveexec_b64 s[4:5], vcc
	s_xor_b64 s[4:5], exec, s[4:5]
	s_cbranch_execz .LBB2_118
	s_mov_b32 s3, 0x298100
	v_cmp_gt_u32_e32 vcc, s3, v2
	s_and_saveexec_b64 s[6:7], vcc
	s_cbranch_execz .LBB2_117
	s_load_dwordx2 s[8:9], s[0:1], 0x38
	v_add_u32_e32 v10, 0xffdb6100, v2
	v_mov_b32_e32 v11, 0
	v_lshlrev_b64 v[2:3], 5, v[10:11]
	s_waitcnt lgkmcnt(0)
	v_lshl_add_u64 v[12:13], s[8:9], 0, v[2:3]
	global_load_dwordx4 v[2:5], v[12:13], off offset:16 nt
	global_load_dwordx4 v[6:9], v[12:13], off nt
	s_load_dwordx2 s[8:9], s[0:1], 0x78
	s_waitcnt vmcnt(1)
	v_cvt_pk_f16_f32 v5, v4, v5
	v_cvt_pk_f16_f32 v4, v2, v3
	s_waitcnt vmcnt(0)
	v_cvt_pk_f16_f32 v3, v8, v9
	v_cvt_pk_f16_f32 v2, v6, v7
	s_waitcnt lgkmcnt(0)
	v_lshl_add_u64 v[6:7], v[10:11], 4, s[8:9]
	global_store_dwordx4 v[6:7], v[2:5], off sc1
	s_nop 1

.LBB2_132:
	s_load_dwordx8 s[4:11], s[0:1], 0x0
	s_load_dwordx2 s[34:35], s[0:1], 0x28
	s_load_dwordx2 s[12:13], s[0:1], 0x20
	v_lshl_or_b32 v34, s2, 14, v0
	s_waitcnt lgkmcnt(0)
	s_mov_b32 s14, 0x61a80
	s_mov_b32 s15, 0xf4240
	s_mov_b32 s16, 0x155cc0
	v_mov_b32_e32 v19, s4
	v_mov_b32_e32 v21, s5
	v_mov_b32_e32 v23, s6
	v_mov_b32_e32 v25, s7
	v_mov_b32_e32 v27, s8
	v_mov_b32_e32 v29, s9
	v_mov_b32_e32 v49, 0
	v_mov_b32_e32 v53, 0
	v_mov_b32_e32 v36, 0x30d40
	v_mov_b32_e32 v38, 0xfff6d840
	v_mov_b32_e32 v32, 0x61a80
	v_mov_b32_e32 v40, 0x61a80
	v_mov_b32_e32 v42, 0xf4240
	v_mov_b32_e32 v44, 0x30d40
	v_mov_b32_e32 v46, 0x61a80
	v_cmp_gt_u32_e64 s[18:19], s14, v34
	v_cmp_gt_u32_e64 s[20:21], s15, v34
	v_cmp_gt_u32_e64 s[22:23], s16, v34
	s_nop 0
	v_cndmask_b32_e64 v50, v27, v23, s[20:21]
	v_cndmask_b32_e64 v50, v50, v19, s[18:19]
	v_cndmask_b32_e64 v51, v29, v25, s[20:21]
	v_cndmask_b32_e64 v51, v51, v21, s[18:19]
	v_cndmask_b32_e64 v48, v38, v36, s[20:21]
	v_cndmask_b32_e64 v48, v48, v32, s[18:19]
	v_add_u32_e32 v48, v48, v34
	v_cndmask_b32_e64 v48, 0, v48, s[22:23]
	v_lshl_add_u64 v[52:53], v[48:49], 2, v[50:51]
	global_load_dword v33, v[52:53], off nt
	v_cndmask_b32_e64 v48, v42, v40, s[20:21]
	v_cndmask_b32_e64 v48, v48, 0, s[18:19]
	v_sub_u32_e32 v48, v34, v48
	v_cndmask_b32_e64 v48, 0, v48, s[22:23]
	v_lshl_add_u64 v[52:53], v[48:49], 2, v[50:51]
	global_load_dword v2, v[52:53], off nt
	v_add_u32_e32 v31, 0x400, v34
	v_cmp_gt_u32_e64 s[18:19], s14, v31
	v_cmp_gt_u32_e64 s[20:21], s15, v31
	v_cmp_gt_u32_e64 s[22:23], s16, v31
	s_nop 0
	v_cndmask_b32_e64 v50, v27, v23, s[20:21]
	v_cndmask_b32_e64 v50, v50, v19, s[18:19]
	v_cndmask_b32_e64 v51, v29, v25, s[20:21]
	v_cndmask_b32_e64 v51, v51, v21, s[18:19]
	v_cndmask_b32_e64 v48, v38, v36, s[20:21]
	v_cndmask_b32_e64 v48, v48, v32, s[18:19]
	v_add_u32_e32 v48, v48, v31
	v_cndmask_b32_e64 v48, 0, v48, s[22:23]
	v_lshl_add_u64 v[52:53], v[48:49], 2, v[50:51]
	global_load_dword v35, v[52:53], off nt
	v_cndmask_b32_e64 v48, v42, v40, s[20:21]
	v_cndmask_b32_e64 v48, v48, 0, s[18:19]
	v_sub_u32_e32 v48, v31, v48
	v_cndmask_b32_e64 v48, 0, v48, s[22:23]
	v_lshl_add_u64 v[52:53], v[48:49], 2, v[50:51]
	global_load_dword v1, v[52:53], off nt
	v_add_u32_e32 v31, 0x800, v34
	v_cmp_gt_u32_e64 s[18:19], s14, v31
	v_cmp_gt_u32_e64 s[20:21], s15, v31
	v_cmp_gt_u32_e64 s[22:23], s16, v31
	s_nop 0
	v_cndmask_b32_e64 v50, v27, v23, s[20:21]
	v_cndmask_b32_e64 v50, v50, v19, s[18:19]
	v_cndmask_b32_e64 v51, v29, v25, s[20:21]
	v_cndmask_b32_e64 v51, v51, v21, s[18:19]
	v_cndmask_b32_e64 v48, v38, v36, s[20:21]
	v_cndmask_b32_e64 v48, v48, v32, s[18:19]
	v_add_u32_e32 v48, v48, v31
	v_cndmask_b32_e64 v48, 0, v48, s[22:23]
	v_lshl_add_u64 v[52:53], v[48:49], 2, v[50:51]
	global_load_dword v6, v[52:53], off nt
	v_cndmask_b32_e64 v48, v42, v40, s[20:21]
	v_cndmask_b32_e64 v48, v48, 0, s[18:19]
	v_sub_u32_e32 v48, v31, v48
	v_cndmask_b32_e64 v48, 0, v48, s[22:23]
	v_lshl_add_u64 v[52:53], v[48:49], 2, v[50:51]
	global_load_dword v4, v[52:53], off nt
	v_add_u32_e32 v31, 0xc00, v34
	v_cmp_gt_u32_e64 s[18:19], s14, v31
	v_cmp_gt_u32_e64 s[20:21], s15, v31
	v_cmp_gt_u32_e64 s[22:23], s16, v31
	s_nop 0
	v_cndmask_b32_e64 v50, v27, v23, s[20:21]
	v_cndmask_b32_e64 v50, v50, v19, s[18:19]
	v_cndmask_b32_e64 v51, v29, v25, s[20:21]
	v_cndmask_b32_e64 v51, v51, v21, s[18:19]
	v_cndmask_b32_e64 v48, v38, v36, s[20:21]
	v_cndmask_b32_e64 v48, v48, v32, s[18:19]
	v_add_u32_e32 v48, v48, v31
	v_cndmask_b32_e64 v48, 0, v48, s[22:23]
	v_lshl_add_u64 v[52:53], v[48:49], 2, v[50:51]
	global_load_dword v37, v[52:53], off nt
	v_cndmask_b32_e64 v48, v42, v40, s[20:21]
	v_cndmask_b32_e64 v48, v48, 0, s[18:19]
	v_sub_u32_e32 v48, v31, v48
	v_cndmask_b32_e64 v48, 0, v48, s[22:23]
	v_lshl_add_u64 v[52:53], v[48:49], 2, v[50:51]
	global_load_dword v3, v[52:53], off nt
	v_add_u32_e32 v31, 0x1000, v34
	v_cmp_gt_u32_e64 s[18:19], s14, v31
	v_cmp_gt_u32_e64 s[20:21], s15, v31
	v_cmp_gt_u32_e64 s[22:23], s16, v31
	s_nop 0
	v_cndmask_b32_e64 v50, v27, v23, s[20:21]
	v_cndmask_b32_e64 v50, v50, v19, s[18:19]
	v_cndmask_b32_e64 v51, v29, v25, s[20:21]
	v_cndmask_b32_e64 v51, v51, v21, s[18:19]
	v_cndmask_b32_e64 v48, v38, v36, s[20:21]
	v_cndmask_b32_e64 v48, v48, v32, s[18:19]
	v_add_u32_e32 v48, v48, v31
	v_cndmask_b32_e64 v48, 0, v48, s[22:23]
	v_lshl_add_u64 v[52:53], v[48:49], 2, v[50:51]
	global_load_dword v10, v[52:53], off nt
	v_cndmask_b32_e64 v48, v42, v40, s[20:21]
	v_cndmask_b32_e64 v48, v48, 0, s[18:19]
	v_sub_u32_e32 v48, v31, v48
	v_cndmask_b32_e64 v48, 0, v48, s[22:23]
	v_lshl_add_u64 v[52:53], v[48:49], 2, v[50:51]
	global_load_dword v8, v[52:53], off nt
	v_add_u32_e32 v31, 0x1400, v34
	v_cmp_gt_u32_e64 s[18:19], s14, v31
	v_cmp_gt_u32_e64 s[20:21], s15, v31
	v_cmp_gt_u32_e64 s[22:23], s16, v31
	s_nop 0
	v_cndmask_b32_e64 v50, v27, v23, s[20:21]
	v_cndmask_b32_e64 v50, v50, v19, s[18:19]
	v_cndmask_b32_e64 v51, v29, v25, s[20:21]
	v_cndmask_b32_e64 v51, v51, v21, s[18:19]
	v_cndmask_b32_e64 v48, v38, v36, s[20:21]
	v_cndmask_b32_e64 v48, v48, v32, s[18:19]
	v_add_u32_e32 v48, v48, v31
	v_cndmask_b32_e64 v48, 0, v48, s[22:23]
	v_lshl_add_u64 v[52:53], v[48:49], 2, v[50:51]
	global_load_dword v39, v[52:53], off nt
	v_cndmask_b32_e64 v48, v42, v40, s[20:21]
	v_cndmask_b32_e64 v48, v48, 0, s[18:19]
	v_sub_u32_e32 v48, v31, v48
	v_cndmask_b32_e64 v48, 0, v48, s[22:23]
	v_lshl_add_u64 v[52:53], v[48:49], 2, v[50:51]
	global_load_dword v5, v[52:53], off nt
	v_add_u32_e32 v31, 0x1800, v34
	v_cmp_gt_u32_e64 s[18:19], s14, v31
	v_cmp_gt_u32_e64 s[20:21], s15, v31
	v_cmp_gt_u32_e64 s[22:23], s16, v31
	s_nop 0
	v_cndmask_b32_e64 v50, v27, v23, s[20:21]
	v_cndmask_b32_e64 v50, v50, v19, s[18:19]
	v_cndmask_b32_e64 v51, v29, v25, s[20:21]
	v_cndmask_b32_e64 v51, v51, v21, s[18:19]
	v_cndmask_b32_e64 v48, v38, v36, s[20:21]
	v_cndmask_b32_e64 v48, v48, v32, s[18:19]
	v_add_u32_e32 v48, v48, v31
	v_cndmask_b32_e64 v48, 0, v48, s[22:23]
	v_lshl_add_u64 v[52:53], v[48:49], 2, v[50:51]
	global_load_dword v14, v[52:53], off nt
	v_cndmask_b32_e64 v48, v42, v40, s[20:21]
	v_cndmask_b32_e64 v48, v48, 0, s[18:19]
	v_sub_u32_e32 v48, v31, v48
	v_cndmask_b32_e64 v48, 0, v48, s[22:23]
	v_lshl_add_u64 v[52:53], v[48:49], 2, v[50:51]
	global_load_dword v12, v[52:53], off nt
	v_add_u32_e32 v31, 0x1c00, v34
	v_cmp_gt_u32_e64 s[18:19], s14, v31
	v_cmp_gt_u32_e64 s[20:21], s15, v31
	v_cmp_gt_u32_e64 s[22:23], s16, v31
	s_nop 0
	v_cndmask_b32_e64 v50, v27, v23, s[20:21]
	v_cndmask_b32_e64 v50, v50, v19, s[18:19]
	v_cndmask_b32_e64 v51, v29, v25, s[20:21]
	v_cndmask_b32_e64 v51, v51, v21, s[18:19]
	v_cndmask_b32_e64 v48, v38, v36, s[20:21]
	v_cndmask_b32_e64 v48, v48, v32, s[18:19]
	v_add_u32_e32 v48, v48, v31
	v_cndmask_b32_e64 v48, 0, v48, s[22:23]
	v_lshl_add_u64 v[52:53], v[48:49], 2, v[50:51]
	global_load_dword v41, v[52:53], off nt
	v_cndmask_b32_e64 v48, v42, v40, s[20:21]
	v_cndmask_b32_e64 v48, v48, 0, s[18:19]
	v_sub_u32_e32 v48, v31, v48
	v_cndmask_b32_e64 v48, 0, v48, s[22:23]
	v_lshl_add_u64 v[52:53], v[48:49], 2, v[50:51]
	global_load_dword v7, v[52:53], off nt
	v_add_u32_e32 v31, 0x2000, v34
	v_cmp_gt_u32_e64 s[18:19], s14, v31
	v_cmp_gt_u32_e64 s[20:21], s15, v31
	v_cmp_gt_u32_e64 s[22:23], s16, v31
	s_nop 0
	v_cndmask_b32_e64 v50, v27, v23, s[20:21]
	v_cndmask_b32_e64 v50, v50, v19, s[18:19]
	v_cndmask_b32_e64 v51, v29, v25, s[20:21]
	v_cndmask_b32_e64 v51, v51, v21, s[18:19]
	v_cndmask_b32_e64 v48, v38, v36, s[20:21]
	v_cndmask_b32_e64 v48, v48, v32, s[18:19]
	v_add_u32_e32 v48, v48, v31
	v_cndmask_b32_e64 v48, 0, v48, s[22:23]
	v_lshl_add_u64 v[52:53], v[48:49], 2, v[50:51]
	global_load_dword v18, v[52:53], off nt
	v_cndmask_b32_e64 v48, v42, v40, s[20:21]
	v_cndmask_b32_e64 v48, v48, 0, s[18:19]
	v_sub_u32_e32 v48, v31, v48
	v_cndmask_b32_e64 v48, 0, v48, s[22:23]
	v_lshl_add_u64 v[52:53], v[48:49], 2, v[50:51]
	global_load_dword v16, v[52:53], off nt
	v_add_u32_e32 v31, 0x2400, v34
	v_cmp_gt_u32_e64 s[18:19], s14, v31
	v_cmp_gt_u32_e64 s[20:21], s15, v31
	v_cmp_gt_u32_e64 s[22:23], s16, v31
	s_nop 0
	v_cndmask_b32_e64 v50, v27, v23, s[20:21]
	v_cndmask_b32_e64 v50, v50, v19, s[18:19]
	v_cndmask_b32_e64 v51, v29, v25, s[20:21]
	v_cndmask_b32_e64 v51, v51, v21, s[18:19]
	v_cndmask_b32_e64 v48, v38, v36, s[20:21]
	v_cndmask_b32_e64 v48, v48, v32, s[18:19]
	v_add_u32_e32 v48, v48, v31
	v_cndmask_b32_e64 v48, 0, v48, s[22:23]
	v_lshl_add_u64 v[52:53], v[48:49], 2, v[50:51]
	global_load_dword v43, v[52:53], off nt
	v_cndmask_b32_e64 v48, v42, v40, s[20:21]
	v_cndmask_b32_e64 v48, v48, 0, s[18:19]
	v_sub_u32_e32 v48, v31, v48
	v_cndmask_b32_e64 v48, 0, v48, s[22:23]
	v_lshl_add_u64 v[52:53], v[48:49], 2, v[50:51]
	global_load_dword v9, v[52:53], off nt
	v_add_u32_e32 v31, 0x2800, v34
	v_cmp_gt_u32_e64 s[18:19], s14, v31
	v_cmp_gt_u32_e64 s[20:21], s15, v31
	v_cmp_gt_u32_e64 s[22:23], s16, v31
	s_nop 0
	v_cndmask_b32_e64 v50, v27, v23, s[20:21]
	v_cndmask_b32_e64 v50, v50, v19, s[18:19]
	v_cndmask_b32_e64 v51, v29, v25, s[20:21]
	v_cndmask_b32_e64 v51, v51, v21, s[18:19]
	v_cndmask_b32_e64 v48, v38, v36, s[20:21]
	v_cndmask_b32_e64 v48, v48, v32, s[18:19]
	v_add_u32_e32 v48, v48, v31
	v_cndmask_b32_e64 v48, 0, v48, s[22:23]
	v_lshl_add_u64 v[52:53], v[48:49], 2, v[50:51]
	global_load_dword v22, v[52:53], off nt
	v_cndmask_b32_e64 v48, v42, v40, s[20:21]
	v_cndmask_b32_e64 v48, v48, 0, s[18:19]
	v_sub_u32_e32 v48, v31, v48
	v_cndmask_b32_e64 v48, 0, v48, s[22:23]
	v_lshl_add_u64 v[52:53], v[48:49], 2, v[50:51]
	global_load_dword v20, v[52:53], off nt
	v_add_u32_e32 v31, 0x2c00, v34
	v_cmp_gt_u32_e64 s[18:19], s14, v31
	v_cmp_gt_u32_e64 s[20:21], s15, v31
	v_cmp_gt_u32_e64 s[22:23], s16, v31
	s_nop 0
	v_cndmask_b32_e64 v50, v27, v23, s[20:21]
	v_cndmask_b32_e64 v50, v50, v19, s[18:19]
	v_cndmask_b32_e64 v51, v29, v25, s[20:21]
	v_cndmask_b32_e64 v51, v51, v21, s[18:19]
	v_cndmask_b32_e64 v48, v38, v36, s[20:21]
	v_cndmask_b32_e64 v48, v48, v32, s[18:19]
	v_add_u32_e32 v48, v48, v31
	v_cndmask_b32_e64 v48, 0, v48, s[22:23]
	v_lshl_add_u64 v[52:53], v[48:49], 2, v[50:51]
	global_load_dword v45, v[52:53], off nt
	v_cndmask_b32_e64 v48, v42, v40, s[20:21]
	v_cndmask_b32_e64 v48, v48, 0, s[18:19]
	v_sub_u32_e32 v48, v31, v48
	v_cndmask_b32_e64 v48, 0, v48, s[22:23]
	v_lshl_add_u64 v[52:53], v[48:49], 2, v[50:51]
	global_load_dword v11, v[52:53], off nt
	v_add_u32_e32 v31, 0x3000, v34
	v_cmp_gt_u32_e64 s[18:19], s14, v31
	v_cmp_gt_u32_e64 s[20:21], s15, v31
	v_cmp_gt_u32_e64 s[22:23], s16, v31
	s_nop 0
	v_cndmask_b32_e64 v50, v27, v23, s[20:21]
	v_cndmask_b32_e64 v50, v50, v19, s[18:19]
	v_cndmask_b32_e64 v51, v29, v25, s[20:21]
	v_cndmask_b32_e64 v51, v51, v21, s[18:19]
	v_cndmask_b32_e64 v48, v38, v36, s[20:21]
	v_cndmask_b32_e64 v48, v48, v32, s[18:19]
	v_add_u32_e32 v48, v48, v31
	v_cndmask_b32_e64 v48, 0, v48, s[22:23]
	v_lshl_add_u64 v[52:53], v[48:49], 2, v[50:51]
	global_load_dword v26, v[52:53], off nt
	v_cndmask_b32_e64 v48, v42, v40, s[20:21]
	v_cndmask_b32_e64 v48, v48, 0, s[18:19]
	v_sub_u32_e32 v48, v31, v48
	v_cndmask_b32_e64 v48, 0, v48, s[22:23]
	v_lshl_add_u64 v[52:53], v[48:49], 2, v[50:51]
	global_load_dword v24, v[52:53], off nt
	v_add_u32_e32 v31, 0x3400, v34
	v_cmp_gt_u32_e64 s[18:19], s14, v31
	v_cmp_gt_u32_e64 s[20:21], s15, v31
	v_cmp_gt_u32_e64 s[22:23], s16, v31
	s_nop 0
	v_cndmask_b32_e64 v50, v27, v23, s[20:21]
	v_cndmask_b32_e64 v50, v50, v19, s[18:19]
	v_cndmask_b32_e64 v51, v29, v25, s[20:21]
	v_cndmask_b32_e64 v51, v51, v21, s[18:19]
	v_cndmask_b32_e64 v48, v38, v36, s[20:21]
	v_cndmask_b32_e64 v48, v48, v32, s[18:19]
	v_add_u32_e32 v48, v48, v31
	v_cndmask_b32_e64 v48, 0, v48, s[22:23]
	v_lshl_add_u64 v[52:53], v[48:49], 2, v[50:51]
	global_load_dword v47, v[52:53], off nt
	v_cndmask_b32_e64 v48, v42, v40, s[20:21]
	v_cndmask_b32_e64 v48, v48, 0, s[18:19]
	v_sub_u32_e32 v48, v31, v48
	v_cndmask_b32_e64 v48, 0, v48, s[22:23]
	v_lshl_add_u64 v[52:53], v[48:49], 2, v[50:51]
	global_load_dword v13, v[52:53], off nt
	v_add_u32_e32 v31, 0x3800, v34
	v_cmp_gt_u32_e64 s[18:19], s14, v31
	v_cmp_gt_u32_e64 s[20:21], s15, v31
	v_cmp_gt_u32_e64 s[22:23], s16, v31
	s_nop 0
	v_cndmask_b32_e64 v50, v27, v23, s[20:21]
	v_cndmask_b32_e64 v50, v50, v19, s[18:19]
	v_cndmask_b32_e64 v51, v29, v25, s[20:21]
	v_cndmask_b32_e64 v51, v51, v21, s[18:19]
	v_cndmask_b32_e64 v48, v38, v36, s[20:21]
	v_cndmask_b32_e64 v48, v48, v32, s[18:19]
	v_add_u32_e32 v48, v48, v31
	v_cndmask_b32_e64 v48, 0, v48, s[22:23]
	v_lshl_add_u64 v[52:53], v[48:49], 2, v[50:51]
	global_load_dword v30, v[52:53], off nt
	v_cndmask_b32_e64 v48, v42, v40, s[20:21]
	v_cndmask_b32_e64 v48, v48, 0, s[18:19]
	v_sub_u32_e32 v48, v31, v48
	v_cndmask_b32_e64 v48, 0, v48, s[22:23]
	v_lshl_add_u64 v[52:53], v[48:49], 2, v[50:51]
	global_load_dword v28, v[52:53], off nt
	v_add_u32_e32 v31, 0x3c00, v34
	v_cmp_gt_u32_e64 s[18:19], s14, v31
	v_cmp_gt_u32_e64 s[20:21], s15, v31
	v_cmp_gt_u32_e64 s[22:23], s16, v31
	s_nop 0
	v_cndmask_b32_e64 v50, v27, v23, s[20:21]
	v_cndmask_b32_e64 v50, v50, v19, s[18:19]
	v_cndmask_b32_e64 v51, v29, v25, s[20:21]
	v_cndmask_b32_e64 v51, v51, v21, s[18:19]
	v_cndmask_b32_e64 v48, v38, v36, s[20:21]
	v_cndmask_b32_e64 v48, v48, v32, s[18:19]
	v_add_u32_e32 v48, v48, v31
	v_cndmask_b32_e64 v48, 0, v48, s[22:23]
	v_lshl_add_u64 v[52:53], v[48:49], 2, v[50:51]
	global_load_dword v17, v[52:53], off nt
	v_cndmask_b32_e64 v48, v42, v40, s[20:21]
	v_cndmask_b32_e64 v48, v48, 0, s[18:19]
	v_sub_u32_e32 v48, v31, v48
	v_cndmask_b32_e64 v48, 0, v48, s[22:23]
	v_lshl_add_u64 v[52:53], v[48:49], 2, v[50:51]
	global_load_dword v15, v[52:53], off nt
	s_waitcnt vmcnt(0)
	v_mov_b32_e32 v50, -1
	v_cmp_gt_u32_e64 s[18:19], s14, v34
	v_cmp_gt_u32_e64 s[20:21], s15, v34
	v_cmp_gt_u32_e64 s[22:23], s16, v34
	s_nop 0
	v_cndmask_b32_e64 v48, v46, v44, s[20:21]
	v_cndmask_b32_e64 v48, v48, 0, s[18:19]
	v_add_u32_e32 v33, v33, v48
	v_cndmask_b32_e64 v33, v50, v33, s[22:23]
	v_cndmask_b32_e64 v2, 0, v2, s[22:23]
	v_add_u32_e32 v31, 0x400, v34
	v_cmp_gt_u32_e64 s[18:19], s14, v31
	v_cmp_gt_u32_e64 s[20:21], s15, v31
	v_cmp_gt_u32_e64 s[22:23], s16, v31
	s_nop 0
	v_cndmask_b32_e64 v48, v46, v44, s[20:21]
	v_cndmask_b32_e64 v48, v48, 0, s[18:19]
	v_add_u32_e32 v35, v35, v48
	v_cndmask_b32_e64 v35, v50, v35, s[22:23]
	v_cndmask_b32_e64 v1, 0, v1, s[22:23]
	v_add_u32_e32 v31, 0x800, v34
	v_cmp_gt_u32_e64 s[18:19], s14, v31
	v_cmp_gt_u32_e64 s[20:21], s15, v31
	v_cmp_gt_u32_e64 s[22:23], s16, v31
	s_nop 0
	v_cndmask_b32_e64 v48, v46, v44, s[20:21]
	v_cndmask_b32_e64 v48, v48, 0, s[18:19]
	v_add_u32_e32 v6, v6, v48
	v_cndmask_b32_e64 v6, v50, v6, s[22:23]
	v_cndmask_b32_e64 v4, 0, v4, s[22:23]
	v_add_u32_e32 v31, 0xc00, v34
	v_cmp_gt_u32_e64 s[18:19], s14, v31
	v_cmp_gt_u32_e64 s[20:21], s15, v31
	v_cmp_gt_u32_e64 s[22:23], s16, v31
	s_nop 0
	v_cndmask_b32_e64 v48, v46, v44, s[20:21]
	v_cndmask_b32_e64 v48, v48, 0, s[18:19]
	v_add_u32_e32 v37, v37, v48
	v_cndmask_b32_e64 v37, v50, v37, s[22:23]
	v_cndmask_b32_e64 v3, 0, v3, s[22:23]
	v_add_u32_e32 v31, 0x1000, v34
	v_cmp_gt_u32_e64 s[18:19], s14, v31
	v_cmp_gt_u32_e64 s[20:21], s15, v31
	v_cmp_gt_u32_e64 s[22:23], s16, v31
	s_nop 0
	v_cndmask_b32_e64 v48, v46, v44, s[20:21]
	v_cndmask_b32_e64 v48, v48, 0, s[18:19]
	v_add_u32_e32 v10, v10, v48
	v_cndmask_b32_e64 v10, v50, v10, s[22:23]
	v_cndmask_b32_e64 v8, 0, v8, s[22:23]
	v_add_u32_e32 v31, 0x1400, v34
	v_cmp_gt_u32_e64 s[18:19], s14, v31
	v_cmp_gt_u32_e64 s[20:21], s15, v31
	v_cmp_gt_u32_e64 s[22:23], s16, v31
	s_nop 0
	v_cndmask_b32_e64 v48, v46, v44, s[20:21]
	v_cndmask_b32_e64 v48, v48, 0, s[18:19]
	v_add_u32_e32 v39, v39, v48
	v_cndmask_b32_e64 v39, v50, v39, s[22:23]
	v_cndmask_b32_e64 v5, 0, v5, s[22:23]
	v_add_u32_e32 v31, 0x1800, v34
	v_cmp_gt_u32_e64 s[18:19], s14, v31
	v_cmp_gt_u32_e64 s[20:21], s15, v31
	v_cmp_gt_u32_e64 s[22:23], s16, v31
	s_nop 0
	v_cndmask_b32_e64 v48, v46, v44, s[20:21]
	v_cndmask_b32_e64 v48, v48, 0, s[18:19]
	v_add_u32_e32 v14, v14, v48
	v_cndmask_b32_e64 v14, v50, v14, s[22:23]
	v_cndmask_b32_e64 v12, 0, v12, s[22:23]
	v_add_u32_e32 v31, 0x1c00, v34
	v_cmp_gt_u32_e64 s[18:19], s14, v31
	v_cmp_gt_u32_e64 s[20:21], s15, v31
	v_cmp_gt_u32_e64 s[22:23], s16, v31
	s_nop 0
	v_cndmask_b32_e64 v48, v46, v44, s[20:21]
	v_cndmask_b32_e64 v48, v48, 0, s[18:19]
	v_add_u32_e32 v41, v41, v48
	v_cndmask_b32_e64 v41, v50, v41, s[22:23]
	v_cndmask_b32_e64 v7, 0, v7, s[22:23]
	v_add_u32_e32 v31, 0x2000, v34
	v_cmp_gt_u32_e64 s[18:19], s14, v31
	v_cmp_gt_u32_e64 s[20:21], s15, v31
	v_cmp_gt_u32_e64 s[22:23], s16, v31
	s_nop 0
	v_cndmask_b32_e64 v48, v46, v44, s[20:21]
	v_cndmask_b32_e64 v48, v48, 0, s[18:19]
	v_add_u32_e32 v18, v18, v48
	v_cndmask_b32_e64 v18, v50, v18, s[22:23]
	v_cndmask_b32_e64 v16, 0, v16, s[22:23]
	v_add_u32_e32 v31, 0x2400, v34
	v_cmp_gt_u32_e64 s[18:19], s14, v31
	v_cmp_gt_u32_e64 s[20:21], s15, v31
	v_cmp_gt_u32_e64 s[22:23], s16, v31
	s_nop 0
	v_cndmask_b32_e64 v48, v46, v44, s[20:21]
	v_cndmask_b32_e64 v48, v48, 0, s[18:19]
	v_add_u32_e32 v43, v43, v48
	v_cndmask_b32_e64 v43, v50, v43, s[22:23]
	v_cndmask_b32_e64 v9, 0, v9, s[22:23]
	v_add_u32_e32 v31, 0x2800, v34
	v_cmp_gt_u32_e64 s[18:19], s14, v31
	v_cmp_gt_u32_e64 s[20:21], s15, v31
	v_cmp_gt_u32_e64 s[22:23], s16, v31
	s_nop 0
	v_cndmask_b32_e64 v48, v46, v44, s[20:21]
	v_cndmask_b32_e64 v48, v48, 0, s[18:19]
	v_add_u32_e32 v22, v22, v48
	v_cndmask_b32_e64 v22, v50, v22, s[22:23]
	v_cndmask_b32_e64 v20, 0, v20, s[22:23]
	v_add_u32_e32 v31, 0x2c00, v34
	v_cmp_gt_u32_e64 s[18:19], s14, v31
	v_cmp_gt_u32_e64 s[20:21], s15, v31
	v_cmp_gt_u32_e64 s[22:23], s16, v31
	s_nop 0
	v_cndmask_b32_e64 v48, v46, v44, s[20:21]
	v_cndmask_b32_e64 v48, v48, 0, s[18:19]
	v_add_u32_e32 v45, v45, v48
	v_cndmask_b32_e64 v45, v50, v45, s[22:23]
	v_cndmask_b32_e64 v11, 0, v11, s[22:23]
	v_add_u32_e32 v31, 0x3000, v34
	v_cmp_gt_u32_e64 s[18:19], s14, v31
	v_cmp_gt_u32_e64 s[20:21], s15, v31
	v_cmp_gt_u32_e64 s[22:23], s16, v31
	s_nop 0
	v_cndmask_b32_e64 v48, v46, v44, s[20:21]
	v_cndmask_b32_e64 v48, v48, 0, s[18:19]
	v_add_u32_e32 v26, v26, v48
	v_cndmask_b32_e64 v26, v50, v26, s[22:23]
	v_cndmask_b32_e64 v24, 0, v24, s[22:23]
	v_add_u32_e32 v31, 0x3400, v34
	v_cmp_gt_u32_e64 s[18:19], s14, v31
	v_cmp_gt_u32_e64 s[20:21], s15, v31
	v_cmp_gt_u32_e64 s[22:23], s16, v31
	s_nop 0
	v_cndmask_b32_e64 v48, v46, v44, s[20:21]
	v_cndmask_b32_e64 v48, v48, 0, s[18:19]
	v_add_u32_e32 v47, v47, v48
	v_cndmask_b32_e64 v47, v50, v47, s[22:23]
	v_cndmask_b32_e64 v13, 0, v13, s[22:23]
	v_add_u32_e32 v31, 0x3800, v34
	v_cmp_gt_u32_e64 s[18:19], s14, v31
	v_cmp_gt_u32_e64 s[20:21], s15, v31
	v_cmp_gt_u32_e64 s[22:23], s16, v31
	s_nop 0
	v_cndmask_b32_e64 v48, v46, v44, s[20:21]
	v_cndmask_b32_e64 v48, v48, 0, s[18:19]
	v_add_u32_e32 v30, v30, v48
	v_cndmask_b32_e64 v30, v50, v30, s[22:23]
	v_cndmask_b32_e64 v28, 0, v28, s[22:23]
	v_add_u32_e32 v31, 0x3c00, v34
	v_cmp_gt_u32_e64 s[18:19], s14, v31
	v_cmp_gt_u32_e64 s[20:21], s15, v31
	v_cmp_gt_u32_e64 s[22:23], s16, v31
	s_nop 0
	v_cndmask_b32_e64 v48, v46, v44, s[20:21]
	v_cndmask_b32_e64 v48, v48, 0, s[18:19]
	v_add_u32_e32 v17, v17, v48
	v_cndmask_b32_e64 v17, v50, v17, s[22:23]
	v_cndmask_b32_e64 v15, 0, v15, s[22:23]
	s_mov_b64 s[0:1], exec
